# baseline (speedup 1.0000x reference)
.LBB0_14:
	s_waitcnt vmcnt(0)
	v_cvt_pk_bf16_f32 v21, v54, v58
	v_cvt_pk_bf16_f32 v20, v38, v42
	v_cvt_pk_bf16_f32 v19, v14, v22
	v_cvt_pk_bf16_f32 v18, v6, v10
	v_cvt_pk_bf16_f32 v33, v55, v59
	v_cvt_pk_bf16_f32 v32, v39, v43
	v_cvt_pk_bf16_f32 v31, v15, v23
	v_cvt_pk_bf16_f32 v30, v7, v11
	v_cvt_pk_bf16_f32 v49, v56, v60
	v_cvt_pk_bf16_f32 v48, v40, v44
	v_cvt_pk_bf16_f32 v47, v16, v24
	v_cvt_pk_bf16_f32 v46, v8, v12
	v_cvt_pk_bf16_f32 v43, v57, v61
	v_cvt_pk_bf16_f32 v42, v41, v45
	v_cvt_pk_bf16_f32 v41, v17, v25
	v_cvt_pk_bf16_f32 v40, v9, v13
	s_waitcnt lgkmcnt(1)
	v_mfma_f32_16x16x32_bf16 v[50:53], v[74:77], v[18:21], v[102:105]
	s_waitcnt lgkmcnt(0)
	v_mfma_f32_16x16x32_bf16 v[18:21], v[82:85], v[18:21], v[110:113]
	v_mfma_f32_16x16x32_bf16 v[62:65], v[74:77], v[30:33], v[94:97]
	v_mfma_f32_16x16x32_bf16 v[30:33], v[82:85], v[30:33], v[106:109]
	v_mfma_f32_16x16x32_bf16 v[66:69], v[74:77], v[46:49], v[90:93]
	v_mfma_f32_16x16x32_bf16 v[46:49], v[82:85], v[46:49], v[98:101]
	v_mfma_f32_16x16x32_bf16 v[10:13], v[74:77], v[40:43], v[70:73]
	v_mfma_f32_16x16x32_bf16 v[6:9], v[82:85], v[40:43], v[86:89]
	s_and_saveexec_b64 s[0:1], s[4:5]
	s_cbranch_execz .LBB0_16
	s_lshr_b32 s2, s2, 4
	v_lshrrev_b32_e32 v22, 1, v128
	v_mad_u64_u32 v[22:23], s[4:5], s2, 48, v[22:23]
	v_ashrrev_i32_e32 v23, 31, v22
	v_lshlrev_b64 v[22:23], 10, v[22:23]
	v_lshlrev_b32_e32 v24, 9, v126
	v_cvt_pk_bf16_f32 v16, v26, v27
	v_and_b32_e32 v26, 31, v132
	v_lshl_add_u64 v[22:23], s[16:17], 0, v[22:23]
	v_and_b32_e32 v24, 0x200, v24
	v_mov_b32_e32 v25, 0
	v_lshl_add_u64 v[22:23], v[22:23], 0, v[24:25]
	v_lshlrev_b32_e32 v24, 4, v26
	v_cvt_pk_bf16_f32 v17, v28, v29
	v_cvt_pk_bf16_f32 v15, v36, v37
	v_cvt_pk_bf16_f32 v14, v34, v35
	v_lshl_add_u64 v[22:23], v[22:23], 0, v[24:25]
	global_store_dwordx4 v[22:23], v[14:17], off nt

.Lseg_rd:
	v_add_u32_e32 v27, 0x10000, v26
	s_lshl_b32 s0, s0, 2
	ds_read_b128 v[10:13], v27 offset:512
	ds_read_b128 v[14:17], v27 offset:528
	ds_read_b128 v[18:21], v27 offset:25600
	ds_read_b128 v[22:25], v27 offset:25616
	ds_read_b128 v[34:37], v27 offset:50688
	ds_read_b128 v[38:41], v27 offset:50704
	s_or_b32 s0, s0, s24
	s_mul_hi_i32 s1, s0, 0x3000
	s_mulk_i32 s0, 0x3000
	s_add_u32 s0, s8, s0
	s_addc_u32 s1, s9, s1
	s_waitcnt lgkmcnt(0)
	s_barrier
	ds_read_b128 v[2:5], v26
	ds_read_b128 v[6:9], v26 offset:16
	v_mov_b32_e32 v1, 0
	s_cmp_eq_u32 s24, 0
	s_waitcnt lgkmcnt(0)
	v_pk_add_f32 v[8:9], v[8:9], 0 op_sel_hi:[1,0]
	v_pk_add_f32 v[4:5], v[4:5], 0 op_sel_hi:[1,0]
	v_pk_add_f32 v[6:7], v[6:7], 0 op_sel_hi:[1,0]
	v_pk_add_f32 v[2:3], v[2:3], 0 op_sel_hi:[1,0]
	v_pk_add_f32 v[4:5], v[4:5], v[12:13]
	v_pk_add_f32 v[8:9], v[8:9], v[16:17]
	v_pk_add_f32 v[2:3], v[2:3], v[10:11]
	v_pk_add_f32 v[6:7], v[6:7], v[14:15]
	v_pk_add_f32 v[8:9], v[8:9], v[24:25]
	v_pk_add_f32 v[4:5], v[4:5], v[20:21]
	v_pk_add_f32 v[6:7], v[6:7], v[22:23]
	v_pk_add_f32 v[2:3], v[2:3], v[18:19]
	v_pk_add_f32 v[10:11], v[4:5], v[36:37]
	v_pk_add_f32 v[4:5], v[8:9], v[40:41]
	v_pk_add_f32 v[8:9], v[2:3], v[34:35]
	v_pk_add_f32 v[6:7], v[6:7], v[38:39]
	v_lshl_add_u64 v[12:13], v[0:1], 4, s[0:1]
	s_cselect_b64 s[0:1], -1, 0
	v_cmp_gt_u32_e32 vcc, 32, v0
	v_cvt_pk_bf16_f32 v5, v4, v5
	v_cvt_pk_bf16_f32 v3, v10, v11
	v_cvt_pk_bf16_f32 v4, v6, v7
	v_cvt_pk_bf16_f32 v2, v8, v9
	s_and_b64 s[0:1], s[0:1], vcc
	global_store_dwordx4 v[12:13], v[2:5], off nt
	s_and_saveexec_b64 s[4:5], s[0:1]
	s_cbranch_execz .LBB0_20
	v_mov_b32_e32 v1, 0x22800
	v_lshl_add_u32 v1, v0, 2, v1
	ds_read2_b32 v[2:3], v1 offset1:32
	ds_read2_b32 v[4:5], v1 offset0:64 offset1:96
	v_lshl_or_b32 v0, s3, 5, v0
	v_ashrrev_i32_e32 v1, 31, v0
	v_lshl_add_u64 v[0:1], v[0:1], 2, s[10:11]
	s_waitcnt lgkmcnt(1)
	v_add_f32_e32 v2, 0, v2
	v_add_f32_e32 v2, v2, v3
	s_waitcnt lgkmcnt(0)
	v_add_f32_e32 v2, v2, v4
	v_add_f32_e32 v2, v2, v5
	global_store_dword v[0:1], v2, off nt
